# P0 weight conversion: the 8 per-element global loads of each conv_weight inner loop are issued back-to-back into distinct VGPRs with one wait and deferred multiply/LDS writes (was load-wait-write seri
# speedup vs baseline: 1.0141x; 1.0141x over previous
; __device__ __forceinline__ void conv_weight(const float* W, int K, int Nsrc, bf16* Bt, int Ndst, const float* gain, const ColMap& cm,
;                                             LAS float* scr, int gw, int ngw, int lane) {
;     ...
;     for (int it = gw; it < nblk * kblk; it += ngw) {
;         const int kb = it / nblk, nb = it % nblk, k0 = kb * 64, n0 = nb * 32;
;         const int sc = cm.src(n0 + (lane & 31));
; #pragma unroll 8
;         for (int i = 0; i < 32; ++i) {
;             const int kk = 2 * i + (lane >> 5);
;             float v = 0.f;
;             if (sc >= 0) v = W[(size_t)(k0 + kk) * Nsrc + sc] * (gain ? gain[k0 + kk] : 1.0f);
;             scr[kk * 33 + (lane & 31)] = v;
;         }
.LBB0_12:
	global_load_dword v215, v[10:11], off
.LBB0_13:
.LBB0_14:
	s_or_b64 exec, exec, s[10:11]
	s_waitcnt vmcnt(0)
	v_mul_f32_e32 v200, v200, v201
	v_mul_f32_e32 v202, v202, v203
	v_mul_f32_e32 v204, v204, v205
	v_mul_f32_e32 v206, v206, v207
	v_mul_f32_e32 v208, v208, v209
	v_mul_f32_e32 v210, v210, v211
	v_mul_f32_e32 v212, v212, v213
	v_mul_f32_e32 v214, v214, v215
	ds_write_b32 v2, v200
	ds_write_b32 v2, v202 offset:264
	ds_write_b32 v2, v204 offset:528
	ds_write_b32 v2, v206 offset:792
	ds_write_b32 v2, v208 offset:1056
	ds_write_b32 v2, v210 offset:1320
	ds_write_b32 v2, v212 offset:1584
	ds_write_b32 v2, v214 offset:1848
	s_add_i32 s22, s22, 16
	v_add_u32_e32 v2, 0x840, v2
	s_cmp_eq_u32 s22, 64
	v_lshl_add_u64 v[10:11], v[10:11], 0, 64
	s_cbranch_scc1 .LBB0_10
.LBB0_15:
	v_mov_b32_e32 v200, 0
	v_mov_b32_e32 v201, 0
	v_mov_b32_e32 v202, 0
	v_mov_b32_e32 v203, 0
	v_mov_b32_e32 v204, 0
	v_mov_b32_e32 v205, 0
	v_mov_b32_e32 v206, 0
	v_mov_b32_e32 v207, 0
	v_mov_b32_e32 v208, 0
	v_mov_b32_e32 v209, 0
	v_mov_b32_e32 v210, 0
	v_mov_b32_e32 v211, 0
	v_mov_b32_e32 v212, 0
	v_mov_b32_e32 v213, 0
	v_mov_b32_e32 v214, 0
	v_mov_b32_e32 v215, 0
	s_and_saveexec_b64 s[10:11], s[2:3]
	s_cbranch_execz .LBB0_20
	v_add_u32_e32 v12, s22, v8
	v_mad_i64_i32 v[22:23], s[24:25], v12, s17, v[6:7]
	global_load_dword v200, v[22:23], off
	s_and_b64 vcc, exec, s[0:1]
	s_cbranch_vccnz .LBB0_18
	v_readlane_b32 s72, v254, 8
	v_ashrrev_i32_e32 v13, 31, v12
	v_readlane_b32 s74, v254, 10
	v_readlane_b32 s75, v254, 11
	v_readlane_b32 s73, v254, 9
	v_readlane_b32 s76, v254, 12
	v_lshl_add_u64 v[12:13], v[12:13], 2, s[74:75]
	global_load_dword v201, v[12:13], off
	v_readlane_b32 s77, v254, 13
	v_readlane_b32 s78, v254, 14
	v_readlane_b32 s79, v254, 15
	v_readlane_b32 s80, v254, 16
	v_readlane_b32 s81, v254, 17
	v_readlane_b32 s82, v254, 18
	v_readlane_b32 s83, v254, 19
	v_readlane_b32 s84, v254, 20
	v_readlane_b32 s85, v254, 21
	v_readlane_b32 s86, v254, 22
	v_readlane_b32 s87, v254, 23
	s_branch .LBB0_19
.LBB0_18:
	v_mov_b32_e32 v201, 1.0
.LBB0_19:
.LBB0_20:
	s_or_b64 exec, exec, s[10:11]
	s_and_saveexec_b64 s[10:11], s[2:3]
	s_cbranch_execz .LBB0_25
	v_add3_u32 v9, v8, s22, 2
	v_mad_i64_i32 v[12:13], s[24:25], v9, s17, v[6:7]
	global_load_dword v202, v[12:13], off
	s_and_b64 vcc, exec, s[0:1]
	s_cbranch_vccnz .LBB0_23
	global_load_dword v203, v[10:11], off offset:-48
	s_branch .LBB0_24
.LBB0_23:
	v_mov_b32_e32 v203, 1.0
.LBB0_24:
.LBB0_25:
	s_or_b64 exec, exec, s[10:11]
	s_and_saveexec_b64 s[10:11], s[2:3]
	s_cbranch_execz .LBB0_30
	v_add3_u32 v9, v8, s22, 4
	v_mad_i64_i32 v[12:13], s[24:25], v9, s17, v[6:7]
	global_load_dword v204, v[12:13], off
	s_and_b64 vcc, exec, s[0:1]
	s_cbranch_vccnz .LBB0_28
	global_load_dword v205, v[10:11], off offset:-40
	s_branch .LBB0_29
.LBB0_28:
	v_mov_b32_e32 v205, 1.0
.LBB0_29:
.LBB0_30:
	s_or_b64 exec, exec, s[10:11]
	s_and_saveexec_b64 s[10:11], s[2:3]
	s_cbranch_execz .LBB0_35
	v_add3_u32 v9, v8, s22, 6
	v_mad_i64_i32 v[12:13], s[24:25], v9, s17, v[6:7]
	global_load_dword v206, v[12:13], off
	s_and_b64 vcc, exec, s[0:1]
	s_cbranch_vccnz .LBB0_33
	global_load_dword v207, v[10:11], off offset:-32
	s_branch .LBB0_34
.LBB0_33:
	v_mov_b32_e32 v207, 1.0
.LBB0_34:
.LBB0_35:
	s_or_b64 exec, exec, s[10:11]
	s_and_saveexec_b64 s[10:11], s[2:3]
	s_cbranch_execz .LBB0_40
	v_add3_u32 v9, v8, s22, 8
	v_mad_i64_i32 v[12:13], s[24:25], v9, s17, v[6:7]
	global_load_dword v208, v[12:13], off
	s_and_b64 vcc, exec, s[0:1]
	s_cbranch_vccnz .LBB0_38
	global_load_dword v209, v[10:11], off offset:-24
	s_branch .LBB0_39
.LBB0_38:
	v_mov_b32_e32 v209, 1.0
.LBB0_39:
.LBB0_40:
	s_or_b64 exec, exec, s[10:11]
	s_and_saveexec_b64 s[10:11], s[2:3]
	s_cbranch_execz .LBB0_45
	v_add3_u32 v9, v8, s22, 10
	v_mad_i64_i32 v[12:13], s[24:25], v9, s17, v[6:7]
	global_load_dword v210, v[12:13], off
	s_and_b64 vcc, exec, s[0:1]
	s_cbranch_vccnz .LBB0_43
	global_load_dword v211, v[10:11], off offset:-16
	s_branch .LBB0_44
.LBB0_43:
	v_mov_b32_e32 v211, 1.0
.LBB0_44:
.LBB0_45:
	s_or_b64 exec, exec, s[10:11]
	s_and_saveexec_b64 s[10:11], s[2:3]
	s_cbranch_execz .LBB0_50
	v_add3_u32 v9, v8, s22, 12
	v_mad_i64_i32 v[12:13], s[24:25], v9, s17, v[6:7]
	global_load_dword v212, v[12:13], off
	s_and_b64 vcc, exec, s[0:1]
	s_cbranch_vccnz .LBB0_48
	global_load_dword v213, v[10:11], off offset:-8
	s_branch .LBB0_49
.LBB0_48:
	v_mov_b32_e32 v213, 1.0
.LBB0_49:
.LBB0_50:
	s_or_b64 exec, exec, s[10:11]
	s_and_saveexec_b64 s[10:11], s[2:3]
	s_cbranch_execz .LBB0_14
	v_add3_u32 v9, v8, s22, 14
	v_mad_i64_i32 v[12:13], s[24:25], v9, s17, v[6:7]
	global_load_dword v214, v[12:13], off
	s_and_b64 vcc, exec, s[0:1]
	s_cbranch_vccz .LBB0_12
	v_mov_b32_e32 v215, 1.0
	s_branch .LBB0_13

; __device__ __forceinline__ void conv_weight(const float* W, int K, int Nsrc, bf16* Bt, int Ndst, const float* gain, const ColMap& cm,
;                                             LAS float* scr, int gw, int ngw, int lane) {
;     ...
;         for (int i = 0; i < 32; ++i) {
;             const int kk = 2 * i + (lane >> 5);
;             float v = 0.f;
;             if (sc >= 0) v = W[(size_t)(k0 + kk) * Nsrc + sc] * (gain ? gain[k0 + kk] : 1.0f);
;             scr[kk * 33 + (lane & 31)] = v;
;         }
.LBB0_61:
	s_or_b64 exec, exec, s[2:3]
	s_waitcnt vmcnt(0)
	ds_write_b32 v4, v200
	ds_write_b32 v4, v202 offset:264
	ds_write_b32 v4, v204 offset:528
	ds_write_b32 v4, v206 offset:792
	ds_write_b32 v4, v208 offset:1056
	ds_write_b32 v4, v210 offset:1320
	ds_write_b32 v4, v212 offset:1584
	ds_write_b32 v4, v214 offset:1848
	s_add_i32 s1, s1, 16
	s_cmp_eq_u32 s1, 64
	v_add_u32_e32 v4, 0x840, v4
	s_cbranch_scc1 .LBB0_59
.LBB0_62:
	v_mov_b32_e32 v200, 0
	v_mov_b32_e32 v202, 0
	v_mov_b32_e32 v204, 0
	v_mov_b32_e32 v206, 0
	v_mov_b32_e32 v208, 0
	v_mov_b32_e32 v210, 0
	v_mov_b32_e32 v212, 0
	v_mov_b32_e32 v214, 0
	s_and_saveexec_b64 s[2:3], vcc
	s_cbranch_execz .LBB0_64
	v_add_u32_e32 v18, s1, v3
	v_ashrrev_i32_e32 v19, 31, v18
	v_lshlrev_b64 v[18:19], 12, v[18:19]
	v_lshl_add_u64 v[18:19], v[8:9], 0, v[18:19]
	global_load_dword v200, v[18:19], off
.LBB0_64:
	s_or_b64 exec, exec, s[2:3]
	s_and_saveexec_b64 s[2:3], vcc
	s_cbranch_execz .LBB0_66
	v_add3_u32 v18, v3, s1, 2
	v_ashrrev_i32_e32 v19, 31, v18
	v_lshlrev_b64 v[18:19], 12, v[18:19]
	v_lshl_add_u64 v[18:19], v[8:9], 0, v[18:19]
	global_load_dword v202, v[18:19], off
.LBB0_66:
	s_or_b64 exec, exec, s[2:3]
	s_and_saveexec_b64 s[2:3], vcc
	s_cbranch_execz .LBB0_68
	v_add3_u32 v18, v3, s1, 4
	v_ashrrev_i32_e32 v19, 31, v18
	v_lshlrev_b64 v[18:19], 12, v[18:19]
	v_lshl_add_u64 v[18:19], v[8:9], 0, v[18:19]
	global_load_dword v204, v[18:19], off
.LBB0_68:
	s_or_b64 exec, exec, s[2:3]
	s_and_saveexec_b64 s[2:3], vcc
	s_cbranch_execz .LBB0_70
	v_add3_u32 v18, v3, s1, 6
	v_ashrrev_i32_e32 v19, 31, v18
	v_lshlrev_b64 v[18:19], 12, v[18:19]
	v_lshl_add_u64 v[18:19], v[8:9], 0, v[18:19]
	global_load_dword v206, v[18:19], off
.LBB0_70:
	s_or_b64 exec, exec, s[2:3]
	s_and_saveexec_b64 s[2:3], vcc
	s_cbranch_execz .LBB0_72
	v_add3_u32 v18, v3, s1, 8
	v_ashrrev_i32_e32 v19, 31, v18
	v_lshlrev_b64 v[18:19], 12, v[18:19]
	v_lshl_add_u64 v[18:19], v[8:9], 0, v[18:19]
	global_load_dword v208, v[18:19], off
.LBB0_72:
	s_or_b64 exec, exec, s[2:3]
	s_and_saveexec_b64 s[2:3], vcc
	s_cbranch_execz .LBB0_74
	v_add3_u32 v18, v3, s1, 10
	v_ashrrev_i32_e32 v19, 31, v18
	v_lshlrev_b64 v[18:19], 12, v[18:19]
	v_lshl_add_u64 v[18:19], v[8:9], 0, v[18:19]
	global_load_dword v210, v[18:19], off
.LBB0_74:
	s_or_b64 exec, exec, s[2:3]
	s_and_saveexec_b64 s[2:3], vcc
	s_cbranch_execz .LBB0_76
	v_add3_u32 v18, v3, s1, 12
	v_ashrrev_i32_e32 v19, 31, v18
	v_lshlrev_b64 v[18:19], 12, v[18:19]
	v_lshl_add_u64 v[18:19], v[8:9], 0, v[18:19]
	global_load_dword v212, v[18:19], off
.LBB0_76:
	s_or_b64 exec, exec, s[2:3]
	s_and_saveexec_b64 s[2:3], vcc
	s_cbranch_execz .LBB0_61
	v_add3_u32 v18, v3, s1, 14
	v_ashrrev_i32_e32 v19, 31, v18
	v_lshlrev_b64 v[18:19], 12, v[18:19]
	v_lshl_add_u64 v[18:19], v[8:9], 0, v[18:19]
	global_load_dword v214, v[18:19], off
	s_branch .LBB0_61

; __device__ __forceinline__ void conv_weight(const float* W, int K, int Nsrc, bf16* Bt, int Ndst, const float* gain, const ColMap& cm,
;                                             LAS float* scr, int gw, int ngw, int lane) {
;     ...
;         for (int i = 0; i < 32; ++i) {
;             const int kk = 2 * i + (lane >> 5);
;             float v = 0.f;
;             if (sc >= 0) v = W[(size_t)(k0 + kk) * Nsrc + sc] * (gain ? gain[k0 + kk] : 1.0f);
;             scr[kk * 33 + (lane & 31)] = v;
;         }
.LBB0_81:
	s_or_b64 exec, exec, s[2:3]
	s_waitcnt vmcnt(0)
	ds_write_b32 v8, v200
	ds_write_b32 v8, v202 offset:264
	ds_write_b32 v8, v204 offset:528
	ds_write_b32 v8, v206 offset:792
	ds_write_b32 v8, v208 offset:1056
	ds_write_b32 v8, v210 offset:1320
	ds_write_b32 v8, v212 offset:1584
	ds_write_b32 v8, v214 offset:1848
	s_add_i32 s1, s1, 16
	s_cmp_eq_u32 s1, 64
	v_add_u32_e32 v8, 0x840, v8
	s_cbranch_scc1 .LBB0_79
.LBB0_82:
	v_mov_b32_e32 v200, 0
	v_mov_b32_e32 v202, 0
	v_mov_b32_e32 v204, 0
	v_mov_b32_e32 v206, 0
	v_mov_b32_e32 v208, 0
	v_mov_b32_e32 v210, 0
	v_mov_b32_e32 v212, 0
	v_mov_b32_e32 v214, 0
	s_and_saveexec_b64 s[2:3], vcc
	s_cbranch_execz .LBB0_84
	v_add_u32_e32 v18, s1, v2
	v_ashrrev_i32_e32 v19, 31, v18
	v_lshlrev_b64 v[18:19], 12, v[18:19]
	v_lshl_add_u64 v[18:19], v[6:7], 0, v[18:19]
	global_load_dword v200, v[18:19], off
.LBB0_84:
	s_or_b64 exec, exec, s[2:3]
	s_and_saveexec_b64 s[2:3], vcc
	s_cbranch_execz .LBB0_86
	v_add3_u32 v18, v2, s1, 2
	v_ashrrev_i32_e32 v19, 31, v18
	v_lshlrev_b64 v[18:19], 12, v[18:19]
	v_lshl_add_u64 v[18:19], v[6:7], 0, v[18:19]
	global_load_dword v202, v[18:19], off
.LBB0_86:
	s_or_b64 exec, exec, s[2:3]
	s_and_saveexec_b64 s[2:3], vcc
	s_cbranch_execz .LBB0_88
	v_add3_u32 v18, v2, s1, 4
	v_ashrrev_i32_e32 v19, 31, v18
	v_lshlrev_b64 v[18:19], 12, v[18:19]
	v_lshl_add_u64 v[18:19], v[6:7], 0, v[18:19]
	global_load_dword v204, v[18:19], off
.LBB0_88:
	s_or_b64 exec, exec, s[2:3]
	s_and_saveexec_b64 s[2:3], vcc
	s_cbranch_execz .LBB0_90
	v_add3_u32 v18, v2, s1, 6
	v_ashrrev_i32_e32 v19, 31, v18
	v_lshlrev_b64 v[18:19], 12, v[18:19]
	v_lshl_add_u64 v[18:19], v[6:7], 0, v[18:19]
	global_load_dword v206, v[18:19], off
.LBB0_90:
	s_or_b64 exec, exec, s[2:3]
	s_and_saveexec_b64 s[2:3], vcc
	s_cbranch_execz .LBB0_92
	v_add3_u32 v18, v2, s1, 8
	v_ashrrev_i32_e32 v19, 31, v18
	v_lshlrev_b64 v[18:19], 12, v[18:19]
	v_lshl_add_u64 v[18:19], v[6:7], 0, v[18:19]
	global_load_dword v208, v[18:19], off
.LBB0_92:
	s_or_b64 exec, exec, s[2:3]
	s_and_saveexec_b64 s[2:3], vcc
	s_cbranch_execz .LBB0_94
	v_add3_u32 v18, v2, s1, 10
	v_ashrrev_i32_e32 v19, 31, v18
	v_lshlrev_b64 v[18:19], 12, v[18:19]
	v_lshl_add_u64 v[18:19], v[6:7], 0, v[18:19]
	global_load_dword v210, v[18:19], off
.LBB0_94:
	s_or_b64 exec, exec, s[2:3]
	s_and_saveexec_b64 s[2:3], vcc
	s_cbranch_execz .LBB0_96
	v_add3_u32 v18, v2, s1, 12
	v_ashrrev_i32_e32 v19, 31, v18
	v_lshlrev_b64 v[18:19], 12, v[18:19]
	v_lshl_add_u64 v[18:19], v[6:7], 0, v[18:19]
	global_load_dword v212, v[18:19], off
.LBB0_96:
	s_or_b64 exec, exec, s[2:3]
	s_and_saveexec_b64 s[2:3], vcc
	s_cbranch_execz .LBB0_81
	v_add3_u32 v18, v2, s1, 14
	v_ashrrev_i32_e32 v19, 31, v18
	v_lshlrev_b64 v[18:19], 12, v[18:19]
	v_lshl_add_u64 v[18:19], v[6:7], 0, v[18:19]
	global_load_dword v214, v[18:19], off
	s_branch .LBB0_81

; __device__ __forceinline__ void conv_weight(const float* W, int K, int Nsrc, bf16* Bt, int Ndst, const float* gain, const ColMap& cm,
;                                             LAS float* scr, int gw, int ngw, int lane) {
;     ...
;         for (int i = 0; i < 32; ++i) {
;             const int kk = 2 * i + (lane >> 5);
;             float v = 0.f;
;             if (sc >= 0) v = W[(size_t)(k0 + kk) * Nsrc + sc] * (gain ? gain[k0 + kk] : 1.0f);
;             scr[kk * 33 + (lane & 31)] = v;
;         }
.LBB0_122:
	s_or_b64 exec, exec, s[4:5]
	s_waitcnt vmcnt(0)
	ds_write_b32 v8, v200
	ds_write_b32 v8, v202 offset:264
	ds_write_b32 v8, v204 offset:528
	ds_write_b32 v8, v206 offset:792
	ds_write_b32 v8, v208 offset:1056
	ds_write_b32 v8, v210 offset:1320
	ds_write_b32 v8, v212 offset:1584
	ds_write_b32 v8, v214 offset:1848
	s_add_i32 s3, s3, 16
	s_cmp_eq_u32 s3, 64
	v_add_u32_e32 v8, 0x840, v8
	s_cbranch_scc1 .LBB0_120
.LBB0_123:
	v_mov_b32_e32 v200, 0
	v_mov_b32_e32 v202, 0
	v_mov_b32_e32 v204, 0
	v_mov_b32_e32 v206, 0
	v_mov_b32_e32 v208, 0
	v_mov_b32_e32 v210, 0
	v_mov_b32_e32 v212, 0
	v_mov_b32_e32 v214, 0
	s_and_saveexec_b64 s[4:5], vcc
	s_cbranch_execz .LBB0_125
	v_add_u32_e32 v18, s3, v2
	v_ashrrev_i32_e32 v19, 31, v18
	v_lshlrev_b64 v[18:19], 12, v[18:19]
	v_lshl_add_u64 v[18:19], v[6:7], 0, v[18:19]
	global_load_dword v200, v[18:19], off
.LBB0_125:
	s_or_b64 exec, exec, s[4:5]
	s_and_saveexec_b64 s[4:5], vcc
	s_cbranch_execz .LBB0_127
	v_add3_u32 v18, v2, s3, 2
	v_ashrrev_i32_e32 v19, 31, v18
	v_lshlrev_b64 v[18:19], 12, v[18:19]
	v_lshl_add_u64 v[18:19], v[6:7], 0, v[18:19]
	global_load_dword v202, v[18:19], off
.LBB0_127:
	s_or_b64 exec, exec, s[4:5]
	s_and_saveexec_b64 s[4:5], vcc
	s_cbranch_execz .LBB0_129
	v_add3_u32 v18, v2, s3, 4
	v_ashrrev_i32_e32 v19, 31, v18
	v_lshlrev_b64 v[18:19], 12, v[18:19]
	v_lshl_add_u64 v[18:19], v[6:7], 0, v[18:19]
	global_load_dword v204, v[18:19], off
.LBB0_129:
	s_or_b64 exec, exec, s[4:5]
	s_and_saveexec_b64 s[4:5], vcc
	s_cbranch_execz .LBB0_131
	v_add3_u32 v18, v2, s3, 6
	v_ashrrev_i32_e32 v19, 31, v18
	v_lshlrev_b64 v[18:19], 12, v[18:19]
	v_lshl_add_u64 v[18:19], v[6:7], 0, v[18:19]
	global_load_dword v206, v[18:19], off
.LBB0_131:
	s_or_b64 exec, exec, s[4:5]
	s_and_saveexec_b64 s[4:5], vcc
	s_cbranch_execz .LBB0_133
	v_add3_u32 v18, v2, s3, 8
	v_ashrrev_i32_e32 v19, 31, v18
	v_lshlrev_b64 v[18:19], 12, v[18:19]
	v_lshl_add_u64 v[18:19], v[6:7], 0, v[18:19]
	global_load_dword v208, v[18:19], off
.LBB0_133:
	s_or_b64 exec, exec, s[4:5]
	s_and_saveexec_b64 s[4:5], vcc
	s_cbranch_execz .LBB0_135
	v_add3_u32 v18, v2, s3, 10
	v_ashrrev_i32_e32 v19, 31, v18
	v_lshlrev_b64 v[18:19], 12, v[18:19]
	v_lshl_add_u64 v[18:19], v[6:7], 0, v[18:19]
	global_load_dword v210, v[18:19], off
.LBB0_135:
	s_or_b64 exec, exec, s[4:5]
	s_and_saveexec_b64 s[4:5], vcc
	s_cbranch_execz .LBB0_137
	v_add3_u32 v18, v2, s3, 12
	v_ashrrev_i32_e32 v19, 31, v18
	v_lshlrev_b64 v[18:19], 12, v[18:19]
	v_lshl_add_u64 v[18:19], v[6:7], 0, v[18:19]
	global_load_dword v212, v[18:19], off
.LBB0_137:
	s_or_b64 exec, exec, s[4:5]
	s_and_saveexec_b64 s[4:5], vcc
	s_cbranch_execz .LBB0_122
	v_add3_u32 v18, v2, s3, 14
	v_ashrrev_i32_e32 v19, 31, v18
	v_lshlrev_b64 v[18:19], 12, v[18:19]
	v_lshl_add_u64 v[18:19], v[6:7], 0, v[18:19]
	global_load_dword v214, v[18:19], off
	s_branch .LBB0_122

; __device__ __forceinline__ void conv_weight(const float* W, int K, int Nsrc, bf16* Bt, int Ndst, const float* gain, const ColMap& cm,
;                                             LAS float* scr, int gw, int ngw, int lane) {
;     ...
;         for (int i = 0; i < 32; ++i) {
;             const int kk = 2 * i + (lane >> 5);
;             float v = 0.f;
;             if (sc >= 0) v = W[(size_t)(k0 + kk) * Nsrc + sc] * (gain ? gain[k0 + kk] : 1.0f);
;             scr[kk * 33 + (lane & 31)] = v;
;         }
.LBB0_143:
	s_or_b64 exec, exec, s[4:5]
	s_waitcnt vmcnt(0)
	v_mul_f32_e32 v200, v200, v201
	v_mul_f32_e32 v202, v202, v203
	v_mul_f32_e32 v204, v204, v205
	v_mul_f32_e32 v206, v206, v207
	v_mul_f32_e32 v208, v208, v209
	v_mul_f32_e32 v210, v210, v211
	v_mul_f32_e32 v212, v212, v213
	v_mul_f32_e32 v214, v214, v215
	ds_write_b32 v13, v200
	ds_write_b32 v13, v202 offset:264
	ds_write_b32 v13, v204 offset:528
	ds_write_b32 v13, v206 offset:792
	ds_write_b32 v13, v208 offset:1056
	ds_write_b32 v13, v210 offset:1320
	ds_write_b32 v13, v212 offset:1584
	ds_write_b32 v13, v214 offset:1848
	s_add_i32 s3, s3, 16
	s_cmp_eq_u32 s3, 64
	v_add_u32_e32 v13, 0x840, v13
	s_cbranch_scc1 .LBB0_141
.LBB0_144:
	v_mov_b32_e32 v200, 0
	v_mov_b32_e32 v201, 0
	v_mov_b32_e32 v202, 0
	v_mov_b32_e32 v203, 0
	v_mov_b32_e32 v204, 0
	v_mov_b32_e32 v205, 0
	v_mov_b32_e32 v206, 0
	v_mov_b32_e32 v207, 0
	v_mov_b32_e32 v208, 0
	v_mov_b32_e32 v209, 0
	v_mov_b32_e32 v210, 0
	v_mov_b32_e32 v211, 0
	v_mov_b32_e32 v212, 0
	v_mov_b32_e32 v213, 0
	v_mov_b32_e32 v214, 0
	v_mov_b32_e32 v215, 0
	s_and_saveexec_b64 s[4:5], vcc
	s_cbranch_execz .LBB0_146
	v_add_u32_e32 v18, s3, v2
	v_ashrrev_i32_e32 v19, 31, v18
	v_mad_i64_i32 v[20:21], s[16:17], v18, s7, v[6:7]
	v_lshl_add_u64 v[18:19], v[18:19], 2, s[0:1]
	global_load_dword v200, v[20:21], off
	s_nop 0
	global_load_dword v201, v[18:19], off
.LBB0_146:
	s_or_b64 exec, exec, s[4:5]
	s_and_saveexec_b64 s[4:5], vcc
	s_cbranch_execz .LBB0_148
	v_add3_u32 v16, v2, s3, 2
	v_ashrrev_i32_e32 v17, 31, v16
	v_mad_i64_i32 v[18:19], s[16:17], v16, s7, v[6:7]
	v_lshl_add_u64 v[16:17], v[16:17], 2, s[0:1]
	global_load_dword v202, v[18:19], off
	s_nop 0
	global_load_dword v203, v[16:17], off
.LBB0_148:
	s_or_b64 exec, exec, s[4:5]
	s_and_saveexec_b64 s[4:5], vcc
	s_cbranch_execz .LBB0_150
	v_add3_u32 v18, v2, s3, 4
	v_ashrrev_i32_e32 v19, 31, v18
	v_mad_i64_i32 v[20:21], s[16:17], v18, s7, v[6:7]
	v_lshl_add_u64 v[18:19], v[18:19], 2, s[0:1]
	global_load_dword v204, v[20:21], off
	s_nop 0
	global_load_dword v205, v[18:19], off
.LBB0_150:
	s_or_b64 exec, exec, s[4:5]
	s_and_saveexec_b64 s[4:5], vcc
	s_cbranch_execz .LBB0_152
	v_add3_u32 v16, v2, s3, 6
	v_ashrrev_i32_e32 v17, 31, v16
	v_mad_i64_i32 v[18:19], s[16:17], v16, s7, v[6:7]
	v_lshl_add_u64 v[16:17], v[16:17], 2, s[0:1]
	global_load_dword v206, v[18:19], off
	s_nop 0
	global_load_dword v207, v[16:17], off
.LBB0_152:
	s_or_b64 exec, exec, s[4:5]
	s_and_saveexec_b64 s[4:5], vcc
	s_cbranch_execz .LBB0_154
	v_add3_u32 v18, v2, s3, 8
	v_ashrrev_i32_e32 v19, 31, v18
	v_mad_i64_i32 v[20:21], s[16:17], v18, s7, v[6:7]
	v_lshl_add_u64 v[18:19], v[18:19], 2, s[0:1]
	global_load_dword v208, v[20:21], off
	s_nop 0
	global_load_dword v209, v[18:19], off
.LBB0_154:
	s_or_b64 exec, exec, s[4:5]
	s_and_saveexec_b64 s[4:5], vcc
	s_cbranch_execz .LBB0_156
	v_add3_u32 v16, v2, s3, 10
	v_ashrrev_i32_e32 v17, 31, v16
	v_mad_i64_i32 v[18:19], s[16:17], v16, s7, v[6:7]
	v_lshl_add_u64 v[16:17], v[16:17], 2, s[0:1]
	global_load_dword v210, v[18:19], off
	s_nop 0
	global_load_dword v211, v[16:17], off
.LBB0_156:
	s_or_b64 exec, exec, s[4:5]
	s_and_saveexec_b64 s[4:5], vcc
	s_cbranch_execz .LBB0_158
	v_add3_u32 v18, v2, s3, 12
	v_ashrrev_i32_e32 v19, 31, v18
	v_mad_i64_i32 v[20:21], s[16:17], v18, s7, v[6:7]
	v_lshl_add_u64 v[18:19], v[18:19], 2, s[0:1]
	global_load_dword v212, v[20:21], off
	s_nop 0
	global_load_dword v213, v[18:19], off
.LBB0_158:
	s_or_b64 exec, exec, s[4:5]
	s_and_saveexec_b64 s[4:5], vcc
	s_cbranch_execz .LBB0_143
	v_add3_u32 v16, v2, s3, 14
	v_ashrrev_i32_e32 v17, 31, v16
	v_mad_i64_i32 v[18:19], s[16:17], v16, s7, v[6:7]
	v_lshl_add_u64 v[16:17], v[16:17], 2, s[0:1]
	global_load_dword v214, v[18:19], off
	s_nop 0
	global_load_dword v215, v[16:17], off
	s_branch .LBB0_143

; __device__ __forceinline__ void conv_weight(const float* W, int K, int Nsrc, bf16* Bt, int Ndst, const float* gain, const ColMap& cm,
;                                             LAS float* scr, int gw, int ngw, int lane) {
;     ...
;         for (int i = 0; i < 32; ++i) {
;             const int kk = 2 * i + (lane >> 5);
;             float v = 0.f;
;             if (sc >= 0) v = W[(size_t)(k0 + kk) * Nsrc + sc] * (gain ? gain[k0 + kk] : 1.0f);
;             scr[kk * 33 + (lane & 31)] = v;
;         }
.LBB0_165:
.LBB0_166:
	s_or_b64 exec, exec, s[10:11]
	s_waitcnt vmcnt(0)
	v_mul_f32_e32 v200, v200, v201
	v_mul_f32_e32 v202, v202, v203
	v_mul_f32_e32 v204, v204, v205
	v_mul_f32_e32 v206, v206, v207
	v_mul_f32_e32 v208, v208, v209
	v_mul_f32_e32 v210, v210, v211
	v_mul_f32_e32 v212, v212, v213
	v_mul_f32_e32 v214, v214, v215
	ds_write_b32 v2, v200
	ds_write_b32 v2, v202 offset:264
	ds_write_b32 v2, v204 offset:528
	ds_write_b32 v2, v206 offset:792
	ds_write_b32 v2, v208 offset:1056
	ds_write_b32 v2, v210 offset:1320
	ds_write_b32 v2, v212 offset:1584
	ds_write_b32 v2, v214 offset:1848
	s_add_i32 s20, s20, 16
	v_add_u32_e32 v2, 0x840, v2
	s_cmp_eq_u32 s20, 64
	v_lshl_add_u64 v[10:11], v[10:11], 0, 64
	s_cbranch_scc1 .LBB0_162
.LBB0_167:
	v_mov_b32_e32 v200, 0
	v_mov_b32_e32 v201, 0
	v_mov_b32_e32 v202, 0
	v_mov_b32_e32 v203, 0
	v_mov_b32_e32 v204, 0
	v_mov_b32_e32 v205, 0
	v_mov_b32_e32 v206, 0
	v_mov_b32_e32 v207, 0
	v_mov_b32_e32 v208, 0
	v_mov_b32_e32 v209, 0
	v_mov_b32_e32 v210, 0
	v_mov_b32_e32 v211, 0
	v_mov_b32_e32 v212, 0
	v_mov_b32_e32 v213, 0
	v_mov_b32_e32 v214, 0
	v_mov_b32_e32 v215, 0
	s_and_saveexec_b64 s[10:11], s[2:3]
	s_cbranch_execz .LBB0_172
	v_add_u32_e32 v12, s20, v8
	v_mad_i64_i32 v[22:23], s[22:23], v12, s15, v[6:7]
	global_load_dword v200, v[22:23], off
	s_and_b64 vcc, exec, s[0:1]
	s_cbranch_vccnz .LBB0_170
	v_ashrrev_i32_e32 v13, 31, v12
	v_lshl_add_u64 v[12:13], v[12:13], 2, s[64:65]
	global_load_dword v201, v[12:13], off
	s_branch .LBB0_171

; __device__ __forceinline__ void conv_weight(const float* W, int K, int Nsrc, bf16* Bt, int Ndst, const float* gain, const ColMap& cm,
;                                             LAS float* scr, int gw, int ngw, int lane) {
;     ...
;         for (int i = 0; i < 32; ++i) {
;             const int kk = 2 * i + (lane >> 5);
;             float v = 0.f;
;             if (sc >= 0) v = W[(size_t)(k0 + kk) * Nsrc + sc] * (gain ? gain[k0 + kk] : 1.0f);
;             scr[kk * 33 + (lane & 31)] = v;
;         }
.LBB0_171:
.LBB0_172:
	s_or_b64 exec, exec, s[10:11]
	s_and_saveexec_b64 s[10:11], s[2:3]
	s_cbranch_execz .LBB0_177
	v_add3_u32 v9, v8, s20, 2
	v_mad_i64_i32 v[12:13], s[22:23], v9, s15, v[6:7]
	global_load_dword v202, v[12:13], off
	s_and_b64 vcc, exec, s[0:1]
	s_cbranch_vccnz .LBB0_175
	global_load_dword v203, v[10:11], off offset:-48
	s_branch .LBB0_176

; __device__ __forceinline__ void conv_weight(const float* W, int K, int Nsrc, bf16* Bt, int Ndst, const float* gain, const ColMap& cm,
;                                             LAS float* scr, int gw, int ngw, int lane) {
;     ...
;         for (int i = 0; i < 32; ++i) {
;             const int kk = 2 * i + (lane >> 5);
;             float v = 0.f;
;             if (sc >= 0) v = W[(size_t)(k0 + kk) * Nsrc + sc] * (gain ? gain[k0 + kk] : 1.0f);
;             scr[kk * 33 + (lane & 31)] = v;
;         }
.LBB0_176:
.LBB0_177:
	s_or_b64 exec, exec, s[10:11]
	s_and_saveexec_b64 s[10:11], s[2:3]
	s_cbranch_execz .LBB0_182
	v_add3_u32 v9, v8, s20, 4
	v_mad_i64_i32 v[12:13], s[22:23], v9, s15, v[6:7]
	global_load_dword v204, v[12:13], off
	s_and_b64 vcc, exec, s[0:1]
	s_cbranch_vccnz .LBB0_180
	global_load_dword v205, v[10:11], off offset:-40
	s_branch .LBB0_181

; __device__ __forceinline__ void conv_weight(const float* W, int K, int Nsrc, bf16* Bt, int Ndst, const float* gain, const ColMap& cm,
;                                             LAS float* scr, int gw, int ngw, int lane) {
;     ...
;         for (int i = 0; i < 32; ++i) {
;             const int kk = 2 * i + (lane >> 5);
;             float v = 0.f;
;             if (sc >= 0) v = W[(size_t)(k0 + kk) * Nsrc + sc] * (gain ? gain[k0 + kk] : 1.0f);
;             scr[kk * 33 + (lane & 31)] = v;
;         }
.LBB0_181:
.LBB0_182:
	s_or_b64 exec, exec, s[10:11]
	s_and_saveexec_b64 s[10:11], s[2:3]
	s_cbranch_execz .LBB0_187
	v_add3_u32 v9, v8, s20, 6
	v_mad_i64_i32 v[12:13], s[22:23], v9, s15, v[6:7]
	global_load_dword v206, v[12:13], off
	s_and_b64 vcc, exec, s[0:1]
	s_cbranch_vccnz .LBB0_185
	global_load_dword v207, v[10:11], off offset:-32
	s_branch .LBB0_186

; __device__ __forceinline__ void conv_weight(const float* W, int K, int Nsrc, bf16* Bt, int Ndst, const float* gain, const ColMap& cm,
;                                             LAS float* scr, int gw, int ngw, int lane) {
;     ...
;         for (int i = 0; i < 32; ++i) {
;             const int kk = 2 * i + (lane >> 5);
;             float v = 0.f;
;             if (sc >= 0) v = W[(size_t)(k0 + kk) * Nsrc + sc] * (gain ? gain[k0 + kk] : 1.0f);
;             scr[kk * 33 + (lane & 31)] = v;
;         }
.LBB0_186:
.LBB0_187:
	s_or_b64 exec, exec, s[10:11]
	s_and_saveexec_b64 s[10:11], s[2:3]
	s_cbranch_execz .LBB0_192
	v_add3_u32 v9, v8, s20, 8
	v_mad_i64_i32 v[12:13], s[22:23], v9, s15, v[6:7]
	global_load_dword v208, v[12:13], off
	s_and_b64 vcc, exec, s[0:1]
	s_cbranch_vccnz .LBB0_190
	global_load_dword v209, v[10:11], off offset:-24
	s_branch .LBB0_191

; __device__ __forceinline__ void conv_weight(const float* W, int K, int Nsrc, bf16* Bt, int Ndst, const float* gain, const ColMap& cm,
;                                             LAS float* scr, int gw, int ngw, int lane) {
;     ...
;         for (int i = 0; i < 32; ++i) {
;             const int kk = 2 * i + (lane >> 5);
;             float v = 0.f;
;             if (sc >= 0) v = W[(size_t)(k0 + kk) * Nsrc + sc] * (gain ? gain[k0 + kk] : 1.0f);
;             scr[kk * 33 + (lane & 31)] = v;
;         }
.LBB0_191:
.LBB0_192:
	s_or_b64 exec, exec, s[10:11]
	s_and_saveexec_b64 s[10:11], s[2:3]
	s_cbranch_execz .LBB0_197
	v_add3_u32 v9, v8, s20, 10
	v_mad_i64_i32 v[12:13], s[22:23], v9, s15, v[6:7]
	global_load_dword v210, v[12:13], off
	s_and_b64 vcc, exec, s[0:1]
	s_cbranch_vccnz .LBB0_195
	global_load_dword v211, v[10:11], off offset:-16
	s_branch .LBB0_196

; __device__ __forceinline__ void conv_weight(const float* W, int K, int Nsrc, bf16* Bt, int Ndst, const float* gain, const ColMap& cm,
;                                             LAS float* scr, int gw, int ngw, int lane) {
;     ...
;         for (int i = 0; i < 32; ++i) {
;             const int kk = 2 * i + (lane >> 5);
;             float v = 0.f;
;             if (sc >= 0) v = W[(size_t)(k0 + kk) * Nsrc + sc] * (gain ? gain[k0 + kk] : 1.0f);
;             scr[kk * 33 + (lane & 31)] = v;
;         }
.LBB0_196:
.LBB0_197:
	s_or_b64 exec, exec, s[10:11]
	s_and_saveexec_b64 s[10:11], s[2:3]
	s_cbranch_execz .LBB0_202
	v_add3_u32 v9, v8, s20, 12
	v_mad_i64_i32 v[12:13], s[22:23], v9, s15, v[6:7]
	global_load_dword v212, v[12:13], off
	s_and_b64 vcc, exec, s[0:1]
	s_cbranch_vccnz .LBB0_200
	global_load_dword v213, v[10:11], off offset:-8
	s_branch .LBB0_201

; __device__ __forceinline__ void conv_weight(const float* W, int K, int Nsrc, bf16* Bt, int Ndst, const float* gain, const ColMap& cm,
;                                             LAS float* scr, int gw, int ngw, int lane) {
;     ...
;         for (int i = 0; i < 32; ++i) {
;             const int kk = 2 * i + (lane >> 5);
;             float v = 0.f;
;             if (sc >= 0) v = W[(size_t)(k0 + kk) * Nsrc + sc] * (gain ? gain[k0 + kk] : 1.0f);
;             scr[kk * 33 + (lane & 31)] = v;
;         }
.LBB0_201:
.LBB0_202:
	s_or_b64 exec, exec, s[10:11]
	s_and_saveexec_b64 s[10:11], s[2:3]
	s_cbranch_execz .LBB0_166
	v_add3_u32 v9, v8, s20, 14
	v_mad_i64_i32 v[12:13], s[22:23], v9, s15, v[6:7]
	global_load_dword v214, v[12:13], off
	s_and_b64 vcc, exec, s[0:1]
	s_cbranch_vccz .LBB0_164
	v_mov_b32_e32 v215, 1.0
	s_branch .LBB0_165

; __device__ __forceinline__ void conv_weight(const float* W, int K, int Nsrc, bf16* Bt, int Ndst, const float* gain, const ColMap& cm,
;                                             LAS float* scr, int gw, int ngw, int lane) {
;     ...
;         for (int i = 0; i < 32; ++i) {
;             const int kk = 2 * i + (lane >> 5);
;             float v = 0.f;
;             if (sc >= 0) v = W[(size_t)(k0 + kk) * Nsrc + sc] * (gain ? gain[k0 + kk] : 1.0f);
;             scr[kk * 33 + (lane & 31)] = v;
;         }
.LBB0_210:
.LBB0_211:
	s_or_b64 exec, exec, s[10:11]
	s_waitcnt vmcnt(0)
	v_mul_f32_e32 v200, v200, v201
	v_mul_f32_e32 v202, v202, v203
	v_mul_f32_e32 v204, v204, v205
	v_mul_f32_e32 v206, v206, v207
	v_mul_f32_e32 v208, v208, v209
	v_mul_f32_e32 v210, v210, v211
	v_mul_f32_e32 v212, v212, v213
	v_mul_f32_e32 v214, v214, v215
	ds_write_b32 v2, v200
	ds_write_b32 v2, v202 offset:264
	ds_write_b32 v2, v204 offset:528
	ds_write_b32 v2, v206 offset:792
	ds_write_b32 v2, v208 offset:1056
	ds_write_b32 v2, v210 offset:1320
	ds_write_b32 v2, v212 offset:1584
	ds_write_b32 v2, v214 offset:1848
	s_add_i32 s18, s18, 16
	v_add_u32_e32 v2, 0x840, v2
	s_cmp_eq_u32 s18, 64
	v_lshl_add_u64 v[10:11], v[10:11], 0, 64
	s_cbranch_scc1 .LBB0_207
.LBB0_212:
	v_mov_b32_e32 v200, 0
	v_mov_b32_e32 v201, 0
	v_mov_b32_e32 v202, 0
	v_mov_b32_e32 v203, 0
	v_mov_b32_e32 v204, 0
	v_mov_b32_e32 v205, 0
	v_mov_b32_e32 v206, 0
	v_mov_b32_e32 v207, 0
	v_mov_b32_e32 v208, 0
	v_mov_b32_e32 v209, 0
	v_mov_b32_e32 v210, 0
	v_mov_b32_e32 v211, 0
	v_mov_b32_e32 v212, 0
	v_mov_b32_e32 v213, 0
	v_mov_b32_e32 v214, 0
	v_mov_b32_e32 v215, 0
	s_and_saveexec_b64 s[10:11], s[2:3]
	s_cbranch_execz .LBB0_217
	v_add_u32_e32 v12, s18, v8
	v_ashrrev_i32_e32 v13, 31, v12
	v_lshlrev_b64 v[22:23], 12, v[12:13]
	v_lshl_add_u64 v[22:23], v[6:7], 0, v[22:23]
	global_load_dword v200, v[22:23], off
	s_and_b64 vcc, exec, s[0:1]
	s_cbranch_vccnz .LBB0_215
	v_lshl_add_u64 v[12:13], v[12:13], 2, s[68:69]
	global_load_dword v201, v[12:13], off
	s_branch .LBB0_216

; __device__ __forceinline__ void conv_weight(const float* W, int K, int Nsrc, bf16* Bt, int Ndst, const float* gain, const ColMap& cm,
;                                             LAS float* scr, int gw, int ngw, int lane) {
;     ...
;         for (int i = 0; i < 32; ++i) {
;             const int kk = 2 * i + (lane >> 5);
;             float v = 0.f;
;             if (sc >= 0) v = W[(size_t)(k0 + kk) * Nsrc + sc] * (gain ? gain[k0 + kk] : 1.0f);
;             scr[kk * 33 + (lane & 31)] = v;
;         }
.LBB0_216:
.LBB0_217:
	s_or_b64 exec, exec, s[10:11]
	s_and_saveexec_b64 s[10:11], s[2:3]
	s_cbranch_execz .LBB0_222
	v_add3_u32 v12, v8, s18, 2
	v_ashrrev_i32_e32 v13, 31, v12
	v_lshlrev_b64 v[12:13], 12, v[12:13]
	v_lshl_add_u64 v[12:13], v[6:7], 0, v[12:13]
	global_load_dword v202, v[12:13], off
	s_and_b64 vcc, exec, s[0:1]
	s_cbranch_vccnz .LBB0_220
	global_load_dword v203, v[10:11], off offset:-48
	s_branch .LBB0_221

; __device__ __forceinline__ void conv_weight(const float* W, int K, int Nsrc, bf16* Bt, int Ndst, const float* gain, const ColMap& cm,
;                                             LAS float* scr, int gw, int ngw, int lane) {
;     ...
;         for (int i = 0; i < 32; ++i) {
;             const int kk = 2 * i + (lane >> 5);
;             float v = 0.f;
;             if (sc >= 0) v = W[(size_t)(k0 + kk) * Nsrc + sc] * (gain ? gain[k0 + kk] : 1.0f);
;             scr[kk * 33 + (lane & 31)] = v;
;         }
.LBB0_221:
.LBB0_222:
	s_or_b64 exec, exec, s[10:11]
	s_and_saveexec_b64 s[10:11], s[2:3]
	s_cbranch_execz .LBB0_227
	v_add3_u32 v12, v8, s18, 4
	v_ashrrev_i32_e32 v13, 31, v12
	v_lshlrev_b64 v[12:13], 12, v[12:13]
	v_lshl_add_u64 v[12:13], v[6:7], 0, v[12:13]
	global_load_dword v204, v[12:13], off
	s_and_b64 vcc, exec, s[0:1]
	s_cbranch_vccnz .LBB0_225
	global_load_dword v205, v[10:11], off offset:-40
	s_branch .LBB0_226

; __device__ __forceinline__ void conv_weight(const float* W, int K, int Nsrc, bf16* Bt, int Ndst, const float* gain, const ColMap& cm,
;                                             LAS float* scr, int gw, int ngw, int lane) {
;     ...
;         for (int i = 0; i < 32; ++i) {
;             const int kk = 2 * i + (lane >> 5);
;             float v = 0.f;
;             if (sc >= 0) v = W[(size_t)(k0 + kk) * Nsrc + sc] * (gain ? gain[k0 + kk] : 1.0f);
;             scr[kk * 33 + (lane & 31)] = v;
;         }
.LBB0_226:
.LBB0_227:
	s_or_b64 exec, exec, s[10:11]
	s_and_saveexec_b64 s[10:11], s[2:3]
	s_cbranch_execz .LBB0_232
	v_add3_u32 v12, v8, s18, 6
	v_ashrrev_i32_e32 v13, 31, v12
	v_lshlrev_b64 v[12:13], 12, v[12:13]
	v_lshl_add_u64 v[12:13], v[6:7], 0, v[12:13]
	global_load_dword v206, v[12:13], off
	s_and_b64 vcc, exec, s[0:1]
	s_cbranch_vccnz .LBB0_230
	global_load_dword v207, v[10:11], off offset:-32
	s_branch .LBB0_231

; __device__ __forceinline__ void conv_weight(const float* W, int K, int Nsrc, bf16* Bt, int Ndst, const float* gain, const ColMap& cm,
;                                             LAS float* scr, int gw, int ngw, int lane) {
;     ...
;         for (int i = 0; i < 32; ++i) {
;             const int kk = 2 * i + (lane >> 5);
;             float v = 0.f;
;             if (sc >= 0) v = W[(size_t)(k0 + kk) * Nsrc + sc] * (gain ? gain[k0 + kk] : 1.0f);
;             scr[kk * 33 + (lane & 31)] = v;
;         }
.LBB0_231:
.LBB0_232:
	s_or_b64 exec, exec, s[10:11]
	s_and_saveexec_b64 s[10:11], s[2:3]
	s_cbranch_execz .LBB0_237
	v_add3_u32 v12, v8, s18, 8
	v_ashrrev_i32_e32 v13, 31, v12
	v_lshlrev_b64 v[12:13], 12, v[12:13]
	v_lshl_add_u64 v[12:13], v[6:7], 0, v[12:13]
	global_load_dword v208, v[12:13], off
	s_and_b64 vcc, exec, s[0:1]
	s_cbranch_vccnz .LBB0_235
	global_load_dword v209, v[10:11], off offset:-24
	s_branch .LBB0_236

; __device__ __forceinline__ void conv_weight(const float* W, int K, int Nsrc, bf16* Bt, int Ndst, const float* gain, const ColMap& cm,
;                                             LAS float* scr, int gw, int ngw, int lane) {
;     ...
;         for (int i = 0; i < 32; ++i) {
;             const int kk = 2 * i + (lane >> 5);
;             float v = 0.f;
;             if (sc >= 0) v = W[(size_t)(k0 + kk) * Nsrc + sc] * (gain ? gain[k0 + kk] : 1.0f);
;             scr[kk * 33 + (lane & 31)] = v;
;         }
.LBB0_236:
.LBB0_237:
	s_or_b64 exec, exec, s[10:11]
	s_and_saveexec_b64 s[10:11], s[2:3]
	s_cbranch_execz .LBB0_242
	v_add3_u32 v12, v8, s18, 10
	v_ashrrev_i32_e32 v13, 31, v12
	v_lshlrev_b64 v[12:13], 12, v[12:13]
	v_lshl_add_u64 v[12:13], v[6:7], 0, v[12:13]
	global_load_dword v210, v[12:13], off
	s_and_b64 vcc, exec, s[0:1]
	s_cbranch_vccnz .LBB0_240
	global_load_dword v211, v[10:11], off offset:-16
	s_branch .LBB0_241

; __device__ __forceinline__ void conv_weight(const float* W, int K, int Nsrc, bf16* Bt, int Ndst, const float* gain, const ColMap& cm,
;                                             LAS float* scr, int gw, int ngw, int lane) {
;     ...
;         for (int i = 0; i < 32; ++i) {
;             const int kk = 2 * i + (lane >> 5);
;             float v = 0.f;
;             if (sc >= 0) v = W[(size_t)(k0 + kk) * Nsrc + sc] * (gain ? gain[k0 + kk] : 1.0f);
;             scr[kk * 33 + (lane & 31)] = v;
;         }
.LBB0_241:
.LBB0_242:
	s_or_b64 exec, exec, s[10:11]
	s_and_saveexec_b64 s[10:11], s[2:3]
	s_cbranch_execz .LBB0_247
	v_add3_u32 v12, v8, s18, 12
	v_ashrrev_i32_e32 v13, 31, v12
	v_lshlrev_b64 v[12:13], 12, v[12:13]
	v_lshl_add_u64 v[12:13], v[6:7], 0, v[12:13]
	global_load_dword v212, v[12:13], off
	s_and_b64 vcc, exec, s[0:1]
	s_cbranch_vccnz .LBB0_245
	global_load_dword v213, v[10:11], off offset:-8
	s_branch .LBB0_246

; __device__ __forceinline__ void conv_weight(const float* W, int K, int Nsrc, bf16* Bt, int Ndst, const float* gain, const ColMap& cm,
;                                             LAS float* scr, int gw, int ngw, int lane) {
;     ...
;         for (int i = 0; i < 32; ++i) {
;             const int kk = 2 * i + (lane >> 5);
;             float v = 0.f;
;             if (sc >= 0) v = W[(size_t)(k0 + kk) * Nsrc + sc] * (gain ? gain[k0 + kk] : 1.0f);
;             scr[kk * 33 + (lane & 31)] = v;
;         }
.LBB0_246:
.LBB0_247:
	s_or_b64 exec, exec, s[10:11]
	s_and_saveexec_b64 s[10:11], s[2:3]
	s_cbranch_execz .LBB0_211
	v_add3_u32 v12, v8, s18, 14
	v_ashrrev_i32_e32 v13, 31, v12
	v_lshlrev_b64 v[12:13], 12, v[12:13]
	v_lshl_add_u64 v[12:13], v[6:7], 0, v[12:13]
	global_load_dword v214, v[12:13], off
	s_and_b64 vcc, exec, s[0:1]
	s_cbranch_vccz .LBB0_209
	v_mov_b32_e32 v215, 1.0
	s_branch .LBB0_210
